# v17
# speedup vs baseline: 1.0015x; 1.0015x over previous
.Lnerf_hid_a3:
	s_waitcnt vmcnt(0) lgkmcnt(0)
	s_barrier
	ds_read_b128 v[224:227], v121 offset:8192
	ds_read_b128 v[228:231], v121 offset:9216
	v_mfma_f32_16x16x32_bf16 v[80:83], v[240:243], v[48:51], v[80:83]
	ds_read_b128 v[232:235], v121 offset:10240
	v_mfma_f32_16x16x32_bf16 v[76:79], v[244:247], v[48:51], v[76:79]
	ds_read_b128 v[236:239], v121 offset:11264
	v_mfma_f32_16x16x32_bf16 v[72:75], v[244:247], v[52:55], v[72:75]
	v_mfma_f32_16x16x32_bf16 v[84:87], v[240:243], v[52:55], v[84:87]
	ds_read_b128 v[240:243], v121 offset:12288
	ds_read_b128 v[244:247], v121 offset:13312
	v_mfma_f32_16x16x32_bf16 v[80:83], v[248:251], v[112:115], v[80:83]
	v_mfma_f32_16x16x32_bf16 v[76:79], v[252:255], v[112:115], v[76:79]
	v_mfma_f32_16x16x32_bf16 v[72:75], v[252:255], v[116:119], v[72:75]
	v_mfma_f32_16x16x32_bf16 v[84:87], v[248:251], v[116:119], v[84:87]
	ds_read_b128 v[248:251], v121 offset:14336
	ds_read_b128 v[252:255], v121 offset:15360
	s_setprio 3
	s_waitcnt lgkmcnt(6)
	v_mfma_f32_16x16x32_bf16 v[64:67], v[224:227], v[0:3], v[152:155]
	v_mfma_f32_16x16x32_bf16 v[68:71], v[228:231], v[0:3], v[156:159]
	v_mfma_f32_16x16x32_bf16 v[60:63], v[228:231], v[4:7], v[156:159]
	v_mfma_f32_16x16x32_bf16 v[56:59], v[224:227], v[4:7], v[152:155]
	ds_read_b128 v[224:227], v121 offset:16384
	ds_read_b128 v[228:231], v121 offset:17408
	s_waitcnt lgkmcnt(6)
	ds_read_b128 v[160:163], v183 offset:896
	ds_read_b128 v[164:167], v183 offset:960
	v_mfma_f32_16x16x32_bf16 v[64:67], v[232:235], v[12:15], v[64:67]
	v_mfma_f32_16x16x32_bf16 v[68:71], v[236:239], v[12:15], v[68:71]
	s_mov_b32 m0, s28
	s_add_i32 s51, s50, 0x18000
	s_cmp_eq_u32 s52, 3
	s_cselect_b32 s51, 0x100000, s51
	v_mfma_f32_16x16x32_bf16 v[60:63], v[236:239], v[8:11], v[60:63]
	buffer_load_dwordx4 v125, s[36:39], s51 offen lds
	v_mfma_f32_16x16x32_bf16 v[56:59], v[232:235], v[8:11], v[56:59]
	ds_read_b128 v[232:235], v121 offset:18432
	ds_read_b128 v[236:239], v121 offset:19456
	s_waitcnt lgkmcnt(8)
	v_mfma_f32_16x16x32_bf16 v[64:67], v[240:243], v[16:19], v[64:67]
	v_mfma_f32_16x16x32_bf16 v[68:71], v[244:247], v[16:19], v[68:71]
	s_mov_b32 m0, s29
	s_add_i32 s51, s50, 0x1a000
	s_cmp_eq_u32 s52, 3
	s_cselect_b32 s51, 0x102000, s51
	v_mfma_f32_16x16x32_bf16 v[60:63], v[244:247], v[20:23], v[60:63]
	buffer_load_dwordx4 v125, s[36:39], s51 offen lds
	v_mfma_f32_16x16x32_bf16 v[56:59], v[240:243], v[20:23], v[56:59]
	ds_read_b128 v[240:243], v121 offset:20480
	ds_read_b128 v[244:247], v121 offset:21504
	s_waitcnt lgkmcnt(8)
	v_mfma_f32_16x16x32_bf16 v[64:67], v[248:251], v[24:27], v[64:67]
	v_mfma_f32_16x16x32_bf16 v[68:71], v[252:255], v[24:27], v[68:71]
	s_mov_b32 m0, s33
	s_add_i32 s51, s50, 0x1c000
	s_cmp_eq_u32 s52, 3
	s_cselect_b32 s51, 0x104000, s51
	v_mfma_f32_16x16x32_bf16 v[60:63], v[252:255], v[28:31], v[60:63]
	buffer_load_dwordx4 v125, s[36:39], s51 offen lds
	v_mfma_f32_16x16x32_bf16 v[56:59], v[248:251], v[28:31], v[56:59]
	ds_read_b128 v[248:251], v121 offset:22528
	ds_read_b128 v[252:255], v121 offset:23552
	s_setprio 2
	s_waitcnt lgkmcnt(8)
	v_mfma_f32_16x16x32_bf16 v[64:67], v[224:227], v[32:35], v[64:67]
	v_mfma_f32_16x16x32_bf16 v[68:71], v[228:231], v[32:35], v[68:71]
	s_mov_b32 m0, s34
	s_add_i32 s51, s50, 0x1e000
	s_cmp_eq_u32 s52, 3
	s_cselect_b32 s51, 0x106000, s51
	v_mfma_f32_16x16x32_bf16 v[60:63], v[228:231], v[36:39], v[60:63]
	buffer_load_dwordx4 v125, s[36:39], s51 offen lds
	v_mfma_f32_16x16x32_bf16 v[56:59], v[224:227], v[36:39], v[56:59]
	ds_read_b128 v[224:227], v121 offset:24576
	ds_read_b128 v[228:231], v121 offset:25600
	s_waitcnt lgkmcnt(6)
	v_mfma_f32_16x16x32_bf16 v[64:67], v[232:235], v[40:43], v[64:67]
	v_cvt_pk_bf16_f32 v200, v80, v81
	v_mfma_f32_16x16x32_bf16 v[68:71], v[236:239], v[40:43], v[68:71]
	v_cvt_pk_bf16_f32 v201, v82, v83
	v_mfma_f32_16x16x32_bf16 v[60:63], v[236:239], v[44:47], v[60:63]
	v_cvt_pk_bf16_f32 v202, v76, v77
	v_mfma_f32_16x16x32_bf16 v[56:59], v[232:235], v[44:47], v[56:59]
	v_cvt_pk_bf16_f32 v203, v78, v79
	ds_read_b128 v[232:235], v121 offset:26624
	ds_read_b128 v[236:239], v121 offset:27648
	s_waitcnt lgkmcnt(6)
	ds_read_b128 v[152:155], v183 offset:1024
	ds_read_b128 v[156:159], v183 offset:1088
	v_mfma_f32_16x16x32_bf16 v[64:67], v[240:243], v[48:51], v[64:67]
	v_cvt_pk_bf16_f32 v204, v84, v85
	v_mfma_f32_16x16x32_bf16 v[68:71], v[244:247], v[48:51], v[68:71]
	v_cvt_pk_bf16_f32 v205, v86, v87
	v_mfma_f32_16x16x32_bf16 v[60:63], v[244:247], v[52:55], v[60:63]
	v_cvt_pk_bf16_f32 v206, v72, v73
	v_mfma_f32_16x16x32_bf16 v[56:59], v[240:243], v[52:55], v[56:59]
	v_cvt_pk_bf16_f32 v207, v74, v75
	ds_read_b128 v[240:243], v121 offset:28672
	ds_read_b128 v[244:247], v121 offset:29696
	s_waitcnt lgkmcnt(8)
	v_mfma_f32_16x16x32_bf16 v[64:67], v[248:251], v[112:115], v[64:67]
	v_pk_max_i16 v200, v200, 0
	v_mfma_f32_16x16x32_bf16 v[68:71], v[252:255], v[112:115], v[68:71]
	v_pk_max_i16 v201, v201, 0
	v_mfma_f32_16x16x32_bf16 v[60:63], v[252:255], v[116:119], v[60:63]
	v_pk_max_i16 v202, v202, 0
	v_mfma_f32_16x16x32_bf16 v[56:59], v[248:251], v[116:119], v[56:59]
	v_pk_max_i16 v203, v203, 0
	ds_read_b128 v[248:251], v121 offset:30720
	ds_read_b128 v[252:255], v121 offset:31744
	s_setprio 1
	s_waitcnt lgkmcnt(8)
	v_mfma_f32_16x16x32_bf16 v[80:83], v[224:227], v[0:3], v[160:163]
	v_pk_max_i16 v204, v204, 0
	v_mfma_f32_16x16x32_bf16 v[76:79], v[228:231], v[0:3], v[164:167]
	v_pk_max_i16 v205, v205, 0
	v_mfma_f32_16x16x32_bf16 v[72:75], v[228:231], v[4:7], v[164:167]
	v_pk_max_i16 v206, v206, 0
	v_mfma_f32_16x16x32_bf16 v[84:87], v[224:227], v[4:7], v[160:163]
	v_pk_max_i16 v207, v207, 0
	ds_read_b128 v[224:227], v121 offset:32768
	ds_read_b128 v[228:231], v121 offset:33792
	s_waitcnt lgkmcnt(8)
	v_mfma_f32_16x16x32_bf16 v[80:83], v[232:235], v[12:15], v[80:83]
	v_cvt_pk_bf16_f32 v208, v64, v65
	v_mfma_f32_16x16x32_bf16 v[76:79], v[236:239], v[12:15], v[76:79]
	v_cvt_pk_bf16_f32 v209, v66, v67
	v_mfma_f32_16x16x32_bf16 v[72:75], v[236:239], v[8:11], v[72:75]
	v_cvt_pk_bf16_f32 v210, v68, v69
	v_mfma_f32_16x16x32_bf16 v[84:87], v[232:235], v[8:11], v[84:87]
	v_cvt_pk_bf16_f32 v211, v70, v71
	ds_read_b128 v[232:235], v121 offset:34816
	ds_read_b128 v[236:239], v121 offset:35840
	s_waitcnt lgkmcnt(6)
	v_mfma_f32_16x16x32_bf16 v[80:83], v[240:243], v[16:19], v[80:83]
	v_cvt_pk_bf16_f32 v212, v56, v57
	v_mfma_f32_16x16x32_bf16 v[76:79], v[244:247], v[16:19], v[76:79]
	v_cvt_pk_bf16_f32 v213, v58, v59
	v_mfma_f32_16x16x32_bf16 v[72:75], v[244:247], v[20:23], v[72:75]
	v_cvt_pk_bf16_f32 v214, v60, v61
	v_mfma_f32_16x16x32_bf16 v[84:87], v[240:243], v[20:23], v[84:87]
	v_cvt_pk_bf16_f32 v215, v62, v63
	ds_read_b128 v[240:243], v121 offset:36864
	ds_read_b128 v[244:247], v121 offset:37888
	s_waitcnt lgkmcnt(6)
	v_mfma_f32_16x16x32_bf16 v[80:83], v[248:251], v[24:27], v[80:83]
	v_pk_max_i16 v208, v208, 0
	v_mfma_f32_16x16x32_bf16 v[76:79], v[252:255], v[24:27], v[76:79]
	v_pk_max_i16 v209, v209, 0
	v_mfma_f32_16x16x32_bf16 v[72:75], v[252:255], v[28:31], v[72:75]
	v_pk_max_i16 v210, v210, 0
	v_mfma_f32_16x16x32_bf16 v[84:87], v[248:251], v[28:31], v[84:87]
	v_pk_max_i16 v211, v211, 0
	ds_read_b128 v[248:251], v121 offset:38912
	ds_read_b128 v[252:255], v121 offset:39936
	s_setprio 0
	s_waitcnt lgkmcnt(6)
	v_mfma_f32_16x16x32_bf16 v[80:83], v[224:227], v[32:35], v[80:83]
	v_pk_max_i16 v212, v212, 0
	v_mfma_f32_16x16x32_bf16 v[76:79], v[228:231], v[32:35], v[76:79]
	v_pk_max_i16 v213, v213, 0
	v_mfma_f32_16x16x32_bf16 v[72:75], v[228:231], v[36:39], v[72:75]
	v_pk_max_i16 v214, v214, 0
	v_mfma_f32_16x16x32_bf16 v[84:87], v[224:227], v[36:39], v[84:87]
	v_pk_max_i16 v215, v215, 0
	s_waitcnt lgkmcnt(4)
	v_mfma_f32_16x16x32_bf16 v[80:83], v[232:235], v[40:43], v[80:83]
	v_mfma_f32_16x16x32_bf16 v[76:79], v[236:239], v[40:43], v[76:79]
	v_mfma_f32_16x16x32_bf16 v[72:75], v[236:239], v[44:47], v[72:75]
	v_mfma_f32_16x16x32_bf16 v[84:87], v[232:235], v[44:47], v[84:87]
	s_cmp_eq_u32 s52, 3
	s_cbranch_scc1 .Lnerf_head

.Lnerf_hid_b3:
	s_waitcnt vmcnt(0) lgkmcnt(0)
	s_barrier
	ds_read_b128 v[224:227], v121 offset:8192
	ds_read_b128 v[228:231], v121 offset:9216
	v_mfma_f32_16x16x32_bf16 v[80:83], v[240:243], v[48:51], v[80:83]
	ds_read_b128 v[232:235], v121 offset:10240
	v_mfma_f32_16x16x32_bf16 v[76:79], v[244:247], v[48:51], v[76:79]
	ds_read_b128 v[236:239], v121 offset:11264
	v_mfma_f32_16x16x32_bf16 v[72:75], v[244:247], v[52:55], v[72:75]
	v_mfma_f32_16x16x32_bf16 v[84:87], v[240:243], v[52:55], v[84:87]
	ds_read_b128 v[240:243], v121 offset:12288
	ds_read_b128 v[244:247], v121 offset:13312
	v_mfma_f32_16x16x32_bf16 v[80:83], v[248:251], v[112:115], v[80:83]
	v_mfma_f32_16x16x32_bf16 v[76:79], v[252:255], v[112:115], v[76:79]
	v_mfma_f32_16x16x32_bf16 v[72:75], v[252:255], v[116:119], v[72:75]
	v_mfma_f32_16x16x32_bf16 v[84:87], v[248:251], v[116:119], v[84:87]
	ds_read_b128 v[248:251], v121 offset:14336
	ds_read_b128 v[252:255], v121 offset:15360
	s_setprio 3
	s_waitcnt lgkmcnt(6)
	v_mfma_f32_16x16x32_bf16 v[64:67], v[224:227], v[0:3], v[152:155]
	v_mfma_f32_16x16x32_bf16 v[68:71], v[228:231], v[0:3], v[156:159]
	v_mfma_f32_16x16x32_bf16 v[60:63], v[228:231], v[4:7], v[156:159]
	v_mfma_f32_16x16x32_bf16 v[56:59], v[224:227], v[4:7], v[152:155]
	ds_read_b128 v[224:227], v121 offset:16384
	ds_read_b128 v[228:231], v121 offset:17408
	s_waitcnt lgkmcnt(6)
	ds_read_b128 v[160:163], v183 offset:896
	ds_read_b128 v[164:167], v183 offset:960
	v_mfma_f32_16x16x32_bf16 v[64:67], v[232:235], v[12:15], v[64:67]
	v_cvt_pk_bf16_f32 v200, v80, v81
	v_mfma_f32_16x16x32_bf16 v[68:71], v[236:239], v[12:15], v[68:71]
	v_cvt_pk_bf16_f32 v201, v82, v83
	v_mfma_f32_16x16x32_bf16 v[60:63], v[236:239], v[8:11], v[60:63]
	v_cvt_pk_bf16_f32 v202, v76, v77
	v_mfma_f32_16x16x32_bf16 v[56:59], v[232:235], v[8:11], v[56:59]
	v_cvt_pk_bf16_f32 v203, v78, v79
	ds_read_b128 v[232:235], v121 offset:18432
	ds_read_b128 v[236:239], v121 offset:19456
	s_waitcnt lgkmcnt(8)
	v_mfma_f32_16x16x32_bf16 v[64:67], v[240:243], v[16:19], v[64:67]
	v_cvt_pk_bf16_f32 v204, v84, v85
	v_mfma_f32_16x16x32_bf16 v[68:71], v[244:247], v[16:19], v[68:71]
	v_cvt_pk_bf16_f32 v205, v86, v87
	v_mfma_f32_16x16x32_bf16 v[60:63], v[244:247], v[20:23], v[60:63]
	v_cvt_pk_bf16_f32 v206, v72, v73
	v_mfma_f32_16x16x32_bf16 v[56:59], v[240:243], v[20:23], v[56:59]
	v_cvt_pk_bf16_f32 v207, v74, v75
	ds_read_b128 v[240:243], v121 offset:20480
	ds_read_b128 v[244:247], v121 offset:21504
	s_waitcnt lgkmcnt(8)
	v_mfma_f32_16x16x32_bf16 v[64:67], v[248:251], v[24:27], v[64:67]
	v_pk_max_i16 v200, v200, 0
	v_mfma_f32_16x16x32_bf16 v[68:71], v[252:255], v[24:27], v[68:71]
	v_pk_max_i16 v201, v201, 0
	v_mfma_f32_16x16x32_bf16 v[60:63], v[252:255], v[28:31], v[60:63]
	v_pk_max_i16 v202, v202, 0
	v_mfma_f32_16x16x32_bf16 v[56:59], v[248:251], v[28:31], v[56:59]
	v_pk_max_i16 v203, v203, 0
	ds_read_b128 v[248:251], v121 offset:22528
	ds_read_b128 v[252:255], v121 offset:23552
	s_setprio 2
	s_waitcnt lgkmcnt(8)
	v_mfma_f32_16x16x32_bf16 v[64:67], v[224:227], v[32:35], v[64:67]
	v_pk_max_i16 v204, v204, 0
	v_mfma_f32_16x16x32_bf16 v[68:71], v[228:231], v[32:35], v[68:71]
	v_pk_max_i16 v205, v205, 0
	v_mfma_f32_16x16x32_bf16 v[60:63], v[228:231], v[36:39], v[60:63]
	v_pk_max_i16 v206, v206, 0
	v_mfma_f32_16x16x32_bf16 v[56:59], v[224:227], v[36:39], v[56:59]
	v_pk_max_i16 v207, v207, 0
	ds_read_b128 v[224:227], v121 offset:24576
	ds_read_b128 v[228:231], v121 offset:25600
	s_waitcnt lgkmcnt(6)
	v_mfma_f32_16x16x32_bf16 v[64:67], v[232:235], v[40:43], v[64:67]
	v_mfma_f32_16x16x32_bf16 v[68:71], v[236:239], v[40:43], v[68:71]
	s_mov_b32 m0, s28
	s_add_i32 s51, s50, 0x18000
	s_cmp_eq_u32 s52, 3
	s_cselect_b32 s51, 0x100000, s51
	v_mfma_f32_16x16x32_bf16 v[60:63], v[236:239], v[44:47], v[60:63]
	buffer_load_dwordx4 v125, s[36:39], s51 offen lds
	v_mfma_f32_16x16x32_bf16 v[56:59], v[232:235], v[44:47], v[56:59]
	ds_read_b128 v[232:235], v121 offset:26624
	ds_read_b128 v[236:239], v121 offset:27648
	s_waitcnt lgkmcnt(6)
	ds_read_b128 v[152:155], v183 offset:1024
	ds_read_b128 v[156:159], v183 offset:1088
	v_mfma_f32_16x16x32_bf16 v[64:67], v[240:243], v[48:51], v[64:67]
	v_mfma_f32_16x16x32_bf16 v[68:71], v[244:247], v[48:51], v[68:71]
	s_mov_b32 m0, s29
	s_add_i32 s51, s50, 0x1a000
	s_cmp_eq_u32 s52, 3
	s_cselect_b32 s51, 0x102000, s51
	v_mfma_f32_16x16x32_bf16 v[60:63], v[244:247], v[52:55], v[60:63]
	buffer_load_dwordx4 v125, s[36:39], s51 offen lds
	v_mfma_f32_16x16x32_bf16 v[56:59], v[240:243], v[52:55], v[56:59]
	ds_read_b128 v[240:243], v121 offset:28672
	ds_read_b128 v[244:247], v121 offset:29696
	s_waitcnt lgkmcnt(8)
	v_mfma_f32_16x16x32_bf16 v[64:67], v[248:251], v[112:115], v[64:67]
	v_mfma_f32_16x16x32_bf16 v[68:71], v[252:255], v[112:115], v[68:71]
	s_mov_b32 m0, s33
	s_add_i32 s51, s50, 0x1c000
	s_cmp_eq_u32 s52, 3
	s_cselect_b32 s51, 0x104000, s51
	v_mfma_f32_16x16x32_bf16 v[60:63], v[252:255], v[116:119], v[60:63]
	buffer_load_dwordx4 v125, s[36:39], s51 offen lds
	v_mfma_f32_16x16x32_bf16 v[56:59], v[248:251], v[116:119], v[56:59]
	ds_read_b128 v[248:251], v121 offset:30720
	ds_read_b128 v[252:255], v121 offset:31744
	s_setprio 1
	s_waitcnt lgkmcnt(8)
	v_mfma_f32_16x16x32_bf16 v[80:83], v[224:227], v[0:3], v[160:163]
	v_mfma_f32_16x16x32_bf16 v[76:79], v[228:231], v[0:3], v[164:167]
	s_mov_b32 m0, s34
	s_add_i32 s51, s50, 0x1e000
	s_cmp_eq_u32 s52, 3
	s_cselect_b32 s51, 0x106000, s51
	v_mfma_f32_16x16x32_bf16 v[72:75], v[228:231], v[4:7], v[164:167]
	buffer_load_dwordx4 v125, s[36:39], s51 offen lds
	v_mfma_f32_16x16x32_bf16 v[84:87], v[224:227], v[4:7], v[160:163]
	ds_read_b128 v[224:227], v121 offset:32768
	ds_read_b128 v[228:231], v121 offset:33792
	s_waitcnt lgkmcnt(8)
	v_mfma_f32_16x16x32_bf16 v[80:83], v[232:235], v[12:15], v[80:83]
	v_cvt_pk_bf16_f32 v208, v64, v65
	v_mfma_f32_16x16x32_bf16 v[76:79], v[236:239], v[12:15], v[76:79]
	v_cvt_pk_bf16_f32 v209, v66, v67
	v_mfma_f32_16x16x32_bf16 v[72:75], v[236:239], v[8:11], v[72:75]
	v_cvt_pk_bf16_f32 v210, v68, v69
	v_mfma_f32_16x16x32_bf16 v[84:87], v[232:235], v[8:11], v[84:87]
	v_cvt_pk_bf16_f32 v211, v70, v71
	ds_read_b128 v[232:235], v121 offset:34816
	ds_read_b128 v[236:239], v121 offset:35840
	s_waitcnt lgkmcnt(6)
	v_mfma_f32_16x16x32_bf16 v[80:83], v[240:243], v[16:19], v[80:83]
	v_cvt_pk_bf16_f32 v212, v56, v57
	v_mfma_f32_16x16x32_bf16 v[76:79], v[244:247], v[16:19], v[76:79]
	v_cvt_pk_bf16_f32 v213, v58, v59
	v_mfma_f32_16x16x32_bf16 v[72:75], v[244:247], v[20:23], v[72:75]
	v_cvt_pk_bf16_f32 v214, v60, v61
	v_mfma_f32_16x16x32_bf16 v[84:87], v[240:243], v[20:23], v[84:87]
	v_cvt_pk_bf16_f32 v215, v62, v63
	ds_read_b128 v[240:243], v121 offset:36864
	ds_read_b128 v[244:247], v121 offset:37888
	s_waitcnt lgkmcnt(6)
	v_mfma_f32_16x16x32_bf16 v[80:83], v[248:251], v[24:27], v[80:83]
	v_pk_max_i16 v208, v208, 0
	v_mfma_f32_16x16x32_bf16 v[76:79], v[252:255], v[24:27], v[76:79]
	v_pk_max_i16 v209, v209, 0
	v_mfma_f32_16x16x32_bf16 v[72:75], v[252:255], v[28:31], v[72:75]
	v_pk_max_i16 v210, v210, 0
	v_mfma_f32_16x16x32_bf16 v[84:87], v[248:251], v[28:31], v[84:87]
	v_pk_max_i16 v211, v211, 0
	ds_read_b128 v[248:251], v121 offset:38912
	ds_read_b128 v[252:255], v121 offset:39936
	s_setprio 0
	s_waitcnt lgkmcnt(6)
	v_mfma_f32_16x16x32_bf16 v[80:83], v[224:227], v[32:35], v[80:83]
	v_pk_max_i16 v212, v212, 0
	v_mfma_f32_16x16x32_bf16 v[76:79], v[228:231], v[32:35], v[76:79]
	v_pk_max_i16 v213, v213, 0
	v_mfma_f32_16x16x32_bf16 v[72:75], v[228:231], v[36:39], v[72:75]
	v_pk_max_i16 v214, v214, 0
	v_mfma_f32_16x16x32_bf16 v[84:87], v[224:227], v[36:39], v[84:87]
	v_pk_max_i16 v215, v215, 0
	s_waitcnt lgkmcnt(4)
	v_mfma_f32_16x16x32_bf16 v[80:83], v[232:235], v[40:43], v[80:83]
	v_mfma_f32_16x16x32_bf16 v[76:79], v[236:239], v[40:43], v[76:79]
	v_mfma_f32_16x16x32_bf16 v[72:75], v[236:239], v[44:47], v[72:75]
	v_mfma_f32_16x16x32_bf16 v[84:87], v[232:235], v[44:47], v[84:87]
	s_cmp_eq_u32 s52, 3
	s_cbranch_scc1 .Lnerf_head
